# speedup vs baseline: 1.0004x; 1.0004x over previous
.LBB2_52:
	s_addk_i32 s33, 0xff80
	s_addk_i32 s78, 0xc000
	s_add_u32 s95, s95, 0x100
	s_addc_u32 s96, s96, 0
	s_add_u32 s98, s98, 0x100
	s_addc_u32 s80, s80, 0
	s_add_u32 s81, s81, 0x4000
	s_addc_u32 s94, s94, 0
	s_add_u32 s90, s90, 0x4000
	s_addc_u32 s99, s99, 0
	s_add_u32 s97, s97, 0x4000
	s_addc_u32 s68, s68, 0
	s_add_u32 s0, s0, 0x100
	s_addc_u32 s1, s1, 0
	s_add_u32 s93, s93, 0x100
	s_addc_u32 s91, s91, 0
	s_waitcnt vmcnt(0)
	s_waitcnt vmcnt(0) lgkmcnt(0)
	s_barrier
.LBB2_53:
	s_and_b64 vcc, exec, s[82:83]
	s_cbranch_vccnz .LBB2_55
	s_mov_b32 s69, s79
	s_cmp_lt_u32 s69, s92
	s_cselect_b64 s[84:85], -1, 0
	s_cmp_ge_u32 s69, s92
	s_cbranch_scc0 .LBB2_22
	s_branch .LBB2_23
